# v21 + attention pass prologue de-serialisation: norm-gain dwordx4 pairs of both layers hoisted into free registers with counted vmcnt waits
# speedup vs baseline: 1.0273x; 1.0273x over previous
; __device__ __forceinline__ float bf2f(unsigned b) { return __uint_as_float(b << 16); }
; __device__ __forceinline__ float rsq(float x) { return __builtin_amdgcn_rsqf(x); }
; template <int layer>
; __device__ __forceinline__ void attn_phase(LAS unsigned char* lds) {
;     ...
;                 const size_t tq = (size_t)b * SEQ + qlo + r32;
;                 const bf16* qp = Qs + tq * QLD + h * QHS + hi * 8;
;                 u32x4 raw[NQ];
; #pragma unroll
;                 for (int d0 = 0; d0 < NQ; ++d0) raw[d0] = *(const u32x4*)(qp + d0 * 16);
;                 float ss = 0.f;
; #pragma unroll
;                 for (int d0 = 0; d0 < 8; ++d0)
; #pragma unroll
;                     for (int j = 0; j < 4; ++j) { const float x0 = bf2f(raw[d0][j] & 0xffffu), x1 = bf2f(raw[d0][j] >> 16); ss += x0 * x0 + x1 * x1; }
;                 { auto rr = __builtin_amdgcn_permlane32_swap(__float_as_uint(ss), __float_as_uint(ss), false, false); ss = __uint_as_float(rr[0]) + __uint_as_float(rr[1]); }
;                 const float rn = rsq(ss * (1.0f / 128) + EPS) * C2;
.LBB0_529:
	s_and_b64 s[4:5], s[6:7], exec
	v_readlane_b32 s4, v252, 26
	v_readlane_b32 s5, v252, 28
	s_cselect_b32 s8, s5, s4
	v_readlane_b32 s4, v252, 23
	s_add_i32 s28, s8, s4
	s_ashr_i32 s4, s28, 31
	s_add_u32 s14, s24, s28
	s_addc_u32 s60, s25, s4
	v_or_b32_e32 v28, s14, v180
	s_movk_i32 s4, 0x1800
	v_mad_u64_u32 v[20:21], s[4:5], v28, s4, v[186:187]
	v_mad_i32_i24 v21, s60, v217, v21
	global_load_dwordx4 v[22:25], v[20:21], off
	global_load_dwordx4 v[30:33], v[20:21], off offset:32
	global_load_dwordx4 v[34:37], v[20:21], off offset:64
	global_load_dwordx4 v[38:41], v[20:21], off offset:96
	global_load_dwordx4 v[16:19], v[20:21], off offset:128
	global_load_dwordx4 v[12:15], v[20:21], off offset:160
	global_load_dwordx4 v[8:11], v[20:21], off offset:192
	global_load_dwordx4 v[4:7], v[20:21], off offset:224
	v_readlane_b32 s16, v252, 19
	v_readlane_b32 s17, v252, 20
	s_andn2_b64 vcc, exec, s[18:19]
	s_waitcnt vmcnt(7)
	v_and_b32_e32 v27, 0xffff0000, v22
	v_and_b32_e32 v42, 0xffff0000, v23
	v_lshlrev_b32_e32 v26, 16, v22
	v_lshlrev_b32_e32 v29, 16, v23
	v_and_b32_e32 v44, 0xffff0000, v24
	s_waitcnt vmcnt(3)
	v_lshlrev_b32_e32 v71, 16, v16
	v_and_b32_e32 v72, 0xffff0000, v16
	v_mul_f32_e32 v2, v27, v27
	v_mul_f32_e32 v16, v42, v42
	v_lshlrev_b32_e32 v43, 16, v24
	v_and_b32_e32 v46, 0xffff0000, v25
	v_lshlrev_b32_e32 v73, 16, v17
	v_and_b32_e32 v74, 0xffff0000, v17
	v_mul_f32_e32 v17, v44, v44
	v_fmac_f32_e32 v2, v26, v26
	v_fmac_f32_e32 v16, v29, v29
	v_lshlrev_b32_e32 v45, 16, v25
	v_and_b32_e32 v48, 0xffff0000, v30
	v_mul_f32_e32 v22, v46, v46
	v_fmac_f32_e32 v17, v43, v43
	v_add_f32_e32 v2, v2, v16
	v_lshlrev_b32_e32 v47, 16, v30
	v_and_b32_e32 v50, 0xffff0000, v31
	v_mul_f32_e32 v23, v48, v48
	v_fmac_f32_e32 v22, v45, v45
	v_add_f32_e32 v2, v17, v2
	v_lshlrev_b32_e32 v49, 16, v31
	v_and_b32_e32 v52, 0xffff0000, v32
	v_mul_f32_e32 v24, v50, v50
	v_fmac_f32_e32 v23, v47, v47
	v_add_f32_e32 v2, v22, v2
	v_lshlrev_b32_e32 v51, 16, v32
	v_and_b32_e32 v54, 0xffff0000, v33
	v_mul_f32_e32 v25, v52, v52
	v_fmac_f32_e32 v24, v49, v49
	v_add_f32_e32 v2, v23, v2
	v_lshlrev_b32_e32 v53, 16, v33
	v_and_b32_e32 v56, 0xffff0000, v34
	v_mul_f32_e32 v30, v54, v54
	v_fmac_f32_e32 v25, v51, v51
	v_add_f32_e32 v2, v24, v2
	v_lshlrev_b32_e32 v55, 16, v34
	v_and_b32_e32 v58, 0xffff0000, v35
	v_mul_f32_e32 v31, v56, v56
	v_fmac_f32_e32 v30, v53, v53
	v_add_f32_e32 v2, v25, v2
	v_lshlrev_b32_e32 v57, 16, v35
	v_and_b32_e32 v60, 0xffff0000, v36
	v_mul_f32_e32 v32, v58, v58
	v_fmac_f32_e32 v31, v55, v55
	v_add_f32_e32 v2, v30, v2
	v_lshlrev_b32_e32 v59, 16, v36
	v_and_b32_e32 v62, 0xffff0000, v37
	v_mul_f32_e32 v33, v60, v60
	v_fmac_f32_e32 v32, v57, v57
	v_add_f32_e32 v2, v31, v2
	v_lshlrev_b32_e32 v61, 16, v37
	v_and_b32_e32 v64, 0xffff0000, v38
	v_mul_f32_e32 v34, v62, v62
	v_fmac_f32_e32 v33, v59, v59
	v_add_f32_e32 v2, v32, v2
	v_lshlrev_b32_e32 v63, 16, v38
	v_and_b32_e32 v66, 0xffff0000, v39
	v_mul_f32_e32 v35, v64, v64
	v_fmac_f32_e32 v34, v61, v61
	v_add_f32_e32 v2, v33, v2
	v_lshlrev_b32_e32 v65, 16, v39
	v_and_b32_e32 v68, 0xffff0000, v40
	v_mul_f32_e32 v36, v66, v66
	v_fmac_f32_e32 v35, v63, v63
	v_add_f32_e32 v2, v34, v2
	v_lshlrev_b32_e32 v67, 16, v40
	v_and_b32_e32 v70, 0xffff0000, v41
	v_mul_f32_e32 v37, v68, v68
	v_fmac_f32_e32 v36, v65, v65
	v_add_f32_e32 v2, v35, v2
	v_lshlrev_b32_e32 v69, 16, v41
	v_mul_f32_e32 v38, v70, v70
	v_fmac_f32_e32 v37, v67, v67
	v_add_f32_e32 v2, v36, v2
	v_mul_f32_e32 v39, v72, v72
	v_fmac_f32_e32 v38, v69, v69
	v_add_f32_e32 v2, v37, v2
	v_mul_f32_e32 v40, v74, v74
	v_fmac_f32_e32 v39, v71, v71
	v_add_f32_e32 v2, v38, v2
	v_fmac_f32_e32 v40, v73, v73
	v_add_f32_e32 v2, v39, v2
	v_add_f32_e32 v2, v40, v2
	global_load_dwordx4 v[22:25], v[184:185], off offset:16
	global_load_dwordx4 v[38:41], v[184:185], off
	v_and_b32_e32 v76, 0xffff0000, v18
	v_lshlrev_b32_e32 v75, 16, v18
	v_mul_f32_e32 v16, v76, v76
	v_fmac_f32_e32 v16, v75, v75
	v_and_b32_e32 v78, 0xffff0000, v19
	v_add_f32_e32 v2, v16, v2
	v_lshlrev_b32_e32 v77, 16, v19
	v_mul_f32_e32 v16, v78, v78
	s_waitcnt vmcnt(4)
	v_and_b32_e32 v80, 0xffff0000, v12
	v_fmac_f32_e32 v16, v77, v77
	v_lshlrev_b32_e32 v79, 16, v12
	v_mul_f32_e32 v12, v80, v80
	v_add_f32_e32 v2, v16, v2
	v_fmac_f32_e32 v12, v79, v79
	v_and_b32_e32 v82, 0xffff0000, v13
	v_add_f32_e32 v2, v12, v2
	v_lshlrev_b32_e32 v81, 16, v13
	v_mul_f32_e32 v12, v82, v82
	v_fmac_f32_e32 v12, v81, v81
	v_and_b32_e32 v84, 0xffff0000, v14
	v_add_f32_e32 v2, v12, v2
	v_lshlrev_b32_e32 v83, 16, v14
	v_mul_f32_e32 v12, v84, v84
	v_fmac_f32_e32 v12, v83, v83
	v_and_b32_e32 v86, 0xffff0000, v15
	v_add_f32_e32 v2, v12, v2
	v_lshlrev_b32_e32 v85, 16, v15
	v_mul_f32_e32 v12, v86, v86
	s_waitcnt vmcnt(3)
	v_and_b32_e32 v88, 0xffff0000, v8
	v_fmac_f32_e32 v12, v85, v85
	v_lshlrev_b32_e32 v87, 16, v8
	v_mul_f32_e32 v8, v88, v88
	v_add_f32_e32 v2, v12, v2
	v_fmac_f32_e32 v8, v87, v87
	v_and_b32_e32 v90, 0xffff0000, v9
	v_add_f32_e32 v2, v8, v2
	v_lshlrev_b32_e32 v89, 16, v9
	v_mul_f32_e32 v8, v90, v90
	v_fmac_f32_e32 v8, v89, v89
	v_and_b32_e32 v92, 0xffff0000, v10
	v_add_f32_e32 v2, v8, v2
	v_lshlrev_b32_e32 v91, 16, v10
	v_mul_f32_e32 v8, v92, v92
	v_fmac_f32_e32 v8, v91, v91
	v_and_b32_e32 v94, 0xffff0000, v11
	v_add_f32_e32 v2, v8, v2
	v_lshlrev_b32_e32 v93, 16, v11
	v_mul_f32_e32 v8, v94, v94
	v_fmac_f32_e32 v8, v93, v93
	s_waitcnt vmcnt(2)
; __device__ __forceinline__ float bf2f(unsigned b) { return __uint_as_float(b << 16); }
; __device__ __forceinline__ float rsq(float x) { return __builtin_amdgcn_rsqf(x); }
; __device__ __forceinline__ unsigned cvtpk(float lo, float hi) { unsigned r; asm volatile("v_cvt_pk_bf16_f32 %0, %1, %2" : "=v"(r) : "v"(lo), "v"(hi)); return r; }
; template <int layer>
; __device__ __forceinline__ void attn_phase(LAS unsigned char* lds) {
;     ...
;                 const float rn = rsq(ss * (1.0f / 128) + EPS) * C2;
; #pragma unroll
;                 for (int d0 = 0; d0 < 8; ++d0) { const f32x4 g0 = *(const f32x4*)(qkg + d0 * 16 + hi * 8), g1 = *(const f32x4*)(qkg + d0 * 16 + hi * 8 + 4); u32x4 o;
; #pragma unroll
;                     for (int j = 0; j < 4; ++j) { const float x0 = bf2f(raw[d0][j] & 0xffffu), x1 = bf2f(raw[d0][j] >> 16); const f32x4 gg = j < 2 ? g0 : g1;
;                         o[j] = cvtpk(x0 * rn * gg[(2 * j) & 3], x1 * rn * gg[(2 * j + 1) & 3]); }
;                     qr[d0] = *reinterpret_cast<bf16x8*>(&o); }
	v_and_b32_e32 v30, 0xffff0000, v4
	v_add_f32_e32 v8, v8, v2
	v_lshlrev_b32_e32 v2, 16, v4
	v_mul_f32_e32 v4, v30, v30
	v_and_b32_e32 v32, 0xffff0000, v5
	v_fmac_f32_e32 v4, v2, v2
	v_lshlrev_b32_e32 v31, 16, v5
	v_mul_f32_e32 v5, v32, v32
	v_add_f32_e32 v4, v4, v8
	v_fmac_f32_e32 v5, v31, v31
	v_and_b32_e32 v34, 0xffff0000, v6
	v_add_f32_e32 v4, v5, v4
	v_lshlrev_b32_e32 v33, 16, v6
	v_mul_f32_e32 v5, v34, v34
	v_fmac_f32_e32 v5, v33, v33
	v_and_b32_e32 v36, 0xffff0000, v7
	v_add_f32_e32 v4, v5, v4
	v_lshlrev_b32_e32 v35, 16, v7
	v_mul_f32_e32 v5, v36, v36
	v_fmac_f32_e32 v5, v35, v35
	v_add_f32_e32 v4, v5, v4
	v_mov_b32_e32 v5, v4
	s_nop 1
	v_permlane32_swap_b32_e32 v4, v5
	v_add_f32_e32 v4, v4, v5
	v_fmamk_f32 v4, v4, 0x3c000000, v216
	v_rsq_f32_e32 v37, v4
	global_load_dwordx4 v[4:7], v[20:21], off offset:256
	global_load_dwordx4 v[12:15], v[20:21], off offset:288
	global_load_dwordx4 v[8:11], v[20:21], off offset:320
	global_load_dwordx4 v[16:19], v[20:21], off offset:352
	v_mul_f32_e32 v37, 0x3dd53b94, v37
	v_mul_f32_e32 v20, v37, v26
	v_mul_f32_e32 v21, v37, v27
	s_waitcnt vmcnt(4)
	v_mul_f32_e32 v20, v38, v20
	v_mul_f32_e32 v21, v39, v21
	v_cvt_pk_bf16_f32 v132, v20, v21
	v_mul_f32_e32 v20, v37, v29
	v_mul_f32_e32 v21, v37, v42
	v_mul_f32_e32 v20, v40, v20
	v_mul_f32_e32 v21, v41, v21
	v_cvt_pk_bf16_f32 v133, v20, v21
	v_mul_f32_e32 v20, v37, v43
	v_mul_f32_e32 v21, v37, v44
	v_mul_f32_e32 v20, v22, v20
	v_mul_f32_e32 v21, v23, v21
	v_cvt_pk_bf16_f32 v134, v20, v21
	v_mul_f32_e32 v20, v37, v45
	v_mul_f32_e32 v21, v37, v46
	v_mul_f32_e32 v20, v24, v20
	v_mul_f32_e32 v21, v25, v21
	v_cvt_pk_bf16_f32 v135, v20, v21
	global_load_dwordx4 v[20:23], v[184:185], off offset:64
	global_load_dwordx4 v[24:27], v[184:185], off offset:80
	global_load_dwordx4 v[104:107], v[184:185], off offset:128
	global_load_dwordx4 v[108:111], v[184:185], off offset:144
	global_load_dwordx4 v[112:115], v[184:185], off offset:192
	global_load_dwordx4 v[116:119], v[184:185], off offset:208
	global_load_dwordx4 v[120:123], v[184:185], off offset:256
	global_load_dwordx4 v[124:127], v[184:185], off offset:272
	global_load_dwordx4 v[128:131], v[184:185], off offset:320
	global_load_dwordx4 v[238:241], v[184:185], off offset:336
	global_load_dwordx4 v[242:245], v[184:185], off offset:384
	global_load_dwordx4 v[246:249], v[184:185], off offset:400
	v_mul_f32_e32 v29, v37, v47
	v_mul_f32_e32 v38, v37, v56
	v_mul_f32_e32 v39, v37, v57
	v_mul_f32_e32 v40, v37, v58
	v_mul_f32_e32 v41, v37, v59
	v_mul_f32_e32 v42, v37, v60
	v_mul_f32_e32 v43, v37, v61
	v_mul_f32_e32 v44, v37, v62
	v_mul_f32_e32 v2, v37, v2
	s_waitcnt vmcnt(15)
	v_lshlrev_b32_e32 v60, 16, v7
	s_waitcnt vmcnt(14)
	v_lshlrev_b32_e32 v46, 16, v15
	v_and_b32_e32 v56, 0xffff0000, v13
	s_waitcnt vmcnt(12)
	v_lshlrev_b32_e32 v47, 16, v19
	v_and_b32_e32 v57, 0xffff0000, v17
	v_lshlrev_b32_e32 v59, 16, v16
	v_lshlrev_b32_e32 v58, 16, v12
	v_and_b32_e32 v62, 0xffff0000, v7
	v_and_b32_e32 v7, 0xffff0000, v10
	v_lshlrev_b32_e32 v61, 16, v11
	s_waitcnt vmcnt(11)
	v_mul_f32_e32 v20, v20, v29
	v_mul_f32_e32 v29, v37, v48
	v_mul_f32_e32 v21, v21, v29
	v_cvt_pk_bf16_f32 v136, v20, v21
	v_mul_f32_e32 v20, v37, v49
	v_mul_f32_e32 v21, v37, v50
	v_mul_f32_e32 v20, v22, v20
	v_mul_f32_e32 v21, v23, v21
	v_cvt_pk_bf16_f32 v137, v20, v21
	v_mul_f32_e32 v20, v37, v51
	v_mul_f32_e32 v21, v37, v52
	s_waitcnt vmcnt(10)
	v_mul_f32_e32 v20, v20, v24
	v_mul_f32_e32 v21, v21, v25
	v_cvt_pk_bf16_f32 v138, v20, v21
	v_mul_f32_e32 v20, v37, v53
	v_mul_f32_e32 v21, v37, v54
	v_mul_f32_e32 v20, v20, v26
	v_mul_f32_e32 v21, v21, v27
	v_cvt_pk_bf16_f32 v139, v20, v21
	global_load_dwordx4 v[24:27], v[184:185], off offset:448
	global_load_dwordx4 v[20:23], v[184:185], off offset:464
	v_mul_f32_e32 v29, v37, v55
	v_and_b32_e32 v49, 0xffff0000, v19
	v_and_b32_e32 v48, 0xffff0000, v15
	v_lshlrev_b32_e32 v51, 16, v18
	v_lshlrev_b32_e32 v50, 16, v14
	v_and_b32_e32 v53, 0xffff0000, v18
	v_and_b32_e32 v52, 0xffff0000, v14
	v_mul_f32_e32 v14, v37, v30
	v_mul_f32_e32 v15, v37, v31
	v_mul_f32_e32 v18, v37, v32
	v_mul_f32_e32 v19, v37, v33
	v_mul_f32_e32 v30, v37, v34
	v_mul_f32_e32 v31, v37, v35
	v_mul_f32_e32 v32, v37, v36
	v_lshlrev_b32_e32 v55, 16, v17
	v_lshlrev_b32_e32 v54, 16, v13
	v_and_b32_e32 v17, 0xffff0000, v16
	v_and_b32_e32 v16, 0xffff0000, v12
	s_waitcnt vmcnt(11)
	v_mul_f32_e32 v104, v29, v104
	v_mul_f32_e32 v105, v38, v105
	v_mul_f32_e32 v106, v39, v106
	v_mul_f32_e32 v107, v40, v107
	s_waitcnt vmcnt(10)
	v_mul_f32_e32 v108, v41, v108
	v_mul_f32_e32 v109, v42, v109
	v_mul_f32_e32 v110, v43, v110
	v_mul_f32_e32 v111, v44, v111
	v_cvt_pk_bf16_f32 v140, v104, v105
	v_cvt_pk_bf16_f32 v141, v106, v107
	v_cvt_pk_bf16_f32 v142, v108, v109
	v_cvt_pk_bf16_f32 v143, v110, v111
	v_mul_f32_e32 v29, v37, v63
	v_mul_f32_e32 v38, v37, v64
	v_mul_f32_e32 v39, v37, v65
	v_mul_f32_e32 v40, v37, v66
	v_mul_f32_e32 v41, v37, v67
	v_mul_f32_e32 v42, v37, v68
	v_mul_f32_e32 v43, v37, v69
	v_mul_f32_e32 v44, v37, v70
	v_lshlrev_b32_e32 v65, 16, v10
	v_lshlrev_b32_e32 v10, 16, v5
	v_and_b32_e32 v67, 0xffff0000, v9
	v_and_b32_e32 v66, 0xffff0000, v5
	v_lshlrev_b32_e32 v68, 16, v4
	v_and_b32_e32 v5, 0xffff0000, v8
	v_and_b32_e32 v4, 0xffff0000, v4
	v_and_b32_e32 v63, 0xffff0000, v11
	v_lshlrev_b32_e32 v64, 16, v6
	v_and_b32_e32 v6, 0xffff0000, v6
	v_lshlrev_b32_e32 v11, 16, v9
	v_lshlrev_b32_e32 v69, 16, v8
	v_pk_mul_f32 v[8:9], v[48:49], v[48:49]
	s_waitcnt vmcnt(9)
	v_mul_f32_e32 v112, v29, v112
	v_mul_f32_e32 v113, v38, v113
	v_mul_f32_e32 v114, v39, v114
	v_mul_f32_e32 v115, v40, v115
	s_waitcnt vmcnt(8)
; __device__ __forceinline__ float bf2f(unsigned b) { return __uint_as_float(b << 16); }
; __device__ __forceinline__ float rsq(float x) { return __builtin_amdgcn_rsqf(x); }
; __device__ __forceinline__ unsigned cvtpk(float lo, float hi) { unsigned r; asm volatile("v_cvt_pk_bf16_f32 %0, %1, %2" : "=v"(r) : "v"(lo), "v"(hi)); return r; }
; template <int layer>
; __device__ __forceinline__ void attn_phase(LAS unsigned char* lds) {
;     ...
;                 for (int d0 = 0; d0 < 8; ++d0) { const f32x4 g0 = *(const f32x4*)(qkg + d0 * 16 + hi * 8), g1 = *(const f32x4*)(qkg + d0 * 16 + hi * 8 + 4); u32x4 o;
; #pragma unroll
;                     for (int j = 0; j < 4; ++j) { const float x0 = bf2f(raw[d0][j] & 0xffffu), x1 = bf2f(raw[d0][j] >> 16); const f32x4 gg = j < 2 ? g0 : g1;
;                         o[j] = cvtpk(x0 * rn * gg[(2 * j) & 3], x1 * rn * gg[(2 * j + 1) & 3]); }
;                     qr[d0] = *reinterpret_cast<bf16x8*>(&o); }
;                 if constexpr (layer == 0) {
;                     float xr[4][8]; float s2 = 0.f;
; #pragma unroll
;                     for (int c = 0; c < 4; ++c)
; #pragma unroll
;                         for (int j = 0; j < 4; ++j) { xr[c][2 * j] = bf2f(raw[8 + c][j] & 0xffffu); xr[c][2 * j + 1] = bf2f(raw[8 + c][j] >> 16); s2 += xr[c][2 * j] * xr[c][2 * j] + xr[c][2 * j + 1] * xr[c][2 * j + 1]; }
;                     { auto rr = __builtin_amdgcn_permlane32_swap(__float_as_uint(s2), __float_as_uint(s2), false, false); s2 = __uint_as_float(rr[0]) + __uint_as_float(rr[1]); }
;                     const float r2 = rsq(s2 * (1.0f / 64) + EPS); const float pos = (float)positions[tq];
; #pragma unroll
;                     for (int c = 0; c < 4; ++c) { const f32x4 g0 = *(const f32x4*)(qkg + 128 + c * 16 + hi * 8), g1 = *(const f32x4*)(qkg + 128 + c * 16 + hi * 8 + 4);
; #pragma unroll
;                         for (int j = 0; j < 8; ++j) xr[c][j] *= r2 * (j < 4 ? g0[j & 3] : g1[j & 3]); }
	v_mul_f32_e32 v116, v41, v116
	v_mul_f32_e32 v117, v42, v117
	v_mul_f32_e32 v118, v43, v118
	v_mul_f32_e32 v119, v44, v119
	v_cvt_pk_bf16_f32 v144, v112, v113
	v_cvt_pk_bf16_f32 v145, v114, v115
	v_cvt_pk_bf16_f32 v146, v116, v117
	v_cvt_pk_bf16_f32 v147, v118, v119
	v_mul_f32_e32 v29, v37, v71
	v_mul_f32_e32 v38, v37, v72
	v_mul_f32_e32 v39, v37, v73
	v_mul_f32_e32 v40, v37, v74
	v_mul_f32_e32 v41, v37, v75
	v_mul_f32_e32 v42, v37, v76
	v_mul_f32_e32 v43, v37, v77
	v_mul_f32_e32 v44, v37, v78
	v_mov_b32_e32 v74, v49
	v_mov_b32_e32 v75, v53
	v_mov_b32_e32 v72, v47
	v_mov_b32_e32 v73, v51
	v_pk_mul_f32 v[74:75], v[74:75], v[74:75]
	v_pk_mul_f32 v[76:77], v[56:57], v[56:57]
	v_pk_fma_f32 v[72:73], v[72:73], v[72:73], v[74:75]
	v_pk_mul_f32 v[70:71], v[52:53], v[52:53]
	v_pk_fma_f32 v[76:77], v[54:55], v[54:55], v[76:77]
	v_pk_fma_f32 v[70:71], v[50:51], v[50:51], v[70:71]
	v_pk_fma_f32 v[8:9], v[46:47], v[46:47], v[8:9]
	s_waitcnt vmcnt(7)
	v_mul_f32_e32 v120, v29, v120
	v_mul_f32_e32 v121, v38, v121
	v_mul_f32_e32 v122, v39, v122
	v_mul_f32_e32 v123, v40, v123
	s_waitcnt vmcnt(6)
	v_mul_f32_e32 v124, v41, v124
	v_mul_f32_e32 v125, v42, v125
	v_mul_f32_e32 v126, v43, v126
	v_mul_f32_e32 v127, v44, v127
	v_cvt_pk_bf16_f32 v148, v120, v121
	v_cvt_pk_bf16_f32 v149, v122, v123
	v_cvt_pk_bf16_f32 v150, v124, v125
	v_cvt_pk_bf16_f32 v151, v126, v127
	v_mul_f32_e32 v29, v37, v79
	v_mul_f32_e32 v38, v37, v80
	v_mul_f32_e32 v39, v37, v81
	v_mul_f32_e32 v40, v37, v82
	v_mul_f32_e32 v41, v37, v83
	v_mul_f32_e32 v42, v37, v84
	v_mul_f32_e32 v43, v37, v85
	v_mul_f32_e32 v44, v37, v86
	v_mov_b32_e32 v82, v57
	v_mov_b32_e32 v83, v17
	v_mov_b32_e32 v80, v55
	v_mov_b32_e32 v81, v59
	v_pk_mul_f32 v[82:83], v[82:83], v[82:83]
	v_pk_mul_f32 v[84:85], v[62:63], v[62:63]
	v_pk_fma_f32 v[74:75], v[80:81], v[80:81], v[82:83]
	v_pk_mul_f32 v[78:79], v[16:17], v[16:17]
	v_pk_fma_f32 v[84:85], v[60:61], v[60:61], v[84:85]
	v_pk_fma_f32 v[78:79], v[58:59], v[58:59], v[78:79]
	s_waitcnt vmcnt(5)
	v_mul_f32_e32 v128, v29, v128
	v_mul_f32_e32 v129, v38, v129
	v_mul_f32_e32 v130, v39, v130
	v_mul_f32_e32 v131, v40, v131
	s_waitcnt vmcnt(4)
	v_mul_f32_e32 v238, v41, v238
	v_mul_f32_e32 v239, v42, v239
	v_mul_f32_e32 v240, v43, v240
	v_mul_f32_e32 v241, v44, v241
	v_cvt_pk_bf16_f32 v152, v128, v129
	v_cvt_pk_bf16_f32 v153, v130, v131
	v_cvt_pk_bf16_f32 v154, v238, v239
	v_cvt_pk_bf16_f32 v155, v240, v241
	v_mul_f32_e32 v29, v37, v87
	v_mul_f32_e32 v38, v37, v88
	v_mul_f32_e32 v39, v37, v89
	v_mul_f32_e32 v40, v37, v90
	v_mul_f32_e32 v41, v37, v91
	v_mul_f32_e32 v42, v37, v92
	v_mul_f32_e32 v43, v37, v93
	v_mul_f32_e32 v44, v37, v94
	v_pk_mul_f32 v[88:89], v[66:67], v[66:67]
	v_pk_mul_f32 v[90:91], v[4:5], v[4:5]
	v_pk_mul_f32 v[86:87], v[6:7], v[6:7]
	v_pk_fma_f32 v[88:89], v[10:11], v[10:11], v[88:89]
	v_pk_fma_f32 v[90:91], v[68:69], v[68:69], v[90:91]
	v_pk_fma_f32 v[86:87], v[64:65], v[64:65], v[86:87]
	v_pk_add_f32 v[80:81], v[90:91], v[88:89]
	s_waitcnt vmcnt(3)
	v_mul_f32_e32 v242, v29, v242
	v_mul_f32_e32 v243, v38, v243
	v_mul_f32_e32 v244, v39, v244
	v_mul_f32_e32 v245, v40, v245
	s_waitcnt vmcnt(2)
	v_mul_f32_e32 v246, v41, v246
	v_mul_f32_e32 v247, v42, v247
	v_mul_f32_e32 v248, v43, v248
	v_mul_f32_e32 v249, v44, v249
	v_cvt_pk_bf16_f32 v156, v242, v243
	v_cvt_pk_bf16_f32 v157, v244, v245
	v_cvt_pk_bf16_f32 v158, v246, v247
	v_cvt_pk_bf16_f32 v159, v248, v249
	v_cndmask_b32_e64 v29, 0, 1, s[18:19]
	v_cmp_ne_u32_e64 s[4:5], 1, v29
	v_mov_b32_e32 v29, s60
	v_lshl_add_u64 v[28:29], v[28:29], 2, s[16:17]
	v_pk_add_f32 v[80:81], v[86:87], v[80:81]
	s_waitcnt vmcnt(1)
	v_mul_f32_e32 v14, v14, v25
	v_mul_f32_e32 v15, v15, v26
	v_mul_f32_e32 v18, v18, v27
	s_waitcnt vmcnt(0)
	v_mul_f32_e32 v19, v19, v20
	v_mul_f32_e32 v20, v30, v21
	v_mul_f32_e32 v21, v31, v22
	v_mul_f32_e32 v22, v32, v23
	v_mul_f32_e32 v2, v2, v24
	v_cvt_pk_bf16_f32 v160, v2, v14
	v_cvt_pk_bf16_f32 v161, v15, v18
	v_cvt_pk_bf16_f32 v162, v19, v20
	v_cvt_pk_bf16_f32 v163, v21, v22
	global_load_dword v92, v[28:29], off
	global_load_dwordx4 v[18:21], v[184:185], off offset:576
	global_load_dwordx4 v[22:25], v[184:185], off offset:592
	s_nop 0
	global_load_dwordx4 v[26:29], v[184:185], off offset:704
	global_load_dwordx4 v[30:33], v[184:185], off offset:720
	global_load_dwordx4 v[12:15], v[184:185], off offset:512
	global_load_dwordx4 v[34:37], v[184:185], off offset:528
	global_load_dwordx4 v[38:41], v[184:185], off offset:640
	global_load_dwordx4 v[42:45], v[184:185], off offset:656
	v_pk_add_f32 v[80:81], v[84:85], v[80:81]
	s_nop 0
	v_pk_add_f32 v[78:79], v[78:79], v[80:81]
	s_nop 0
	v_pk_add_f32 v[76:77], v[76:77], v[78:79]
	s_nop 0
	v_pk_add_f32 v[70:71], v[70:71], v[76:77]
	s_nop 0
	v_pk_add_f32 v[8:9], v[8:9], v[70:71]
	s_waitcnt vmcnt(8)
	v_cvt_f32_i32_e32 v70, v92
	v_pk_add_f32 v[8:9], v[90:91], v[8:9] op_sel:[1,0] op_sel_hi:[0,1]
	v_pk_add_f32 v[8:9], v[88:89], v[8:9] op_sel:[1,0] op_sel_hi:[0,1]
	v_pk_add_f32 v[8:9], v[86:87], v[8:9] op_sel:[1,0] op_sel_hi:[0,1]
	v_pk_add_f32 v[8:9], v[84:85], v[8:9] op_sel:[1,0] op_sel_hi:[0,1]
	v_pk_add_f32 v[8:9], v[74:75], v[8:9] op_sel:[1,0] op_sel_hi:[0,1]
	v_pk_add_f32 v[8:9], v[74:75], v[8:9]
	s_nop 0
	v_pk_add_f32 v[8:9], v[72:73], v[8:9] op_sel:[1,0] op_sel_hi:[0,1]
	v_pk_add_f32 v[8:9], v[72:73], v[8:9]
	s_nop 0
	v_mov_b32_e32 v2, v8
	s_nop 1
	v_permlane32_swap_b32_e32 v8, v2
	v_add_f32_e32 v2, v8, v2
	v_fmamk_f32 v2, v2, 0x3c800000, v216
	v_rsq_f32_e32 v2, v2
	s_waitcnt vmcnt(6)
	v_mov_b32_e32 v8, v24
	s_waitcnt vmcnt(4)
; __device__ __forceinline__ float rsq(float x) { return __builtin_amdgcn_rsqf(x); }
; template <int layer>
; __device__ __forceinline__ void attn_phase(LAS unsigned char* lds) {
;     ...
;                     const float r2 = rsq(s2 * (1.0f / 64) + EPS); const float pos = (float)positions[tq];
; #pragma unroll
;                     for (int c = 0; c < 4; ++c) { const f32x4 g0 = *(const f32x4*)(qkg + 128 + c * 16 + hi * 8), g1 = *(const f32x4*)(qkg + 128 + c * 16 + hi * 8 + 4);
; #pragma unroll
;                         for (int j = 0; j < 8; ++j) xr[c][j] *= r2 * (j < 4 ? g0[j & 3] : g1[j & 3]); }
; #pragma unroll
;                     for (int c = 0; c < 2; ++c) { u32x4 o1, o2;
; #pragma unroll
;                         for (int jj = 0; jj < 4; ++jj) { float y1[2], y2[2];
; #pragma unroll
;                             for (int e = 0; e < 2; ++e) { const int j = 2 * jj + e; const int i = c * 16 + hi * 8 + j;
;                                 const float freq = exp2f(-(float)i * (13.287712379549449f / 32.0f)); float rev = pos * freq * 0.15915494309189535f; rev -= floorf(rev);
;                                 const float sn = __builtin_amdgcn_sinf(rev), cs = __builtin_amdgcn_cosf(rev);
;                                 y1[e] = (xr[c][j] * cs - xr[c + 2][j] * sn) * C2; y2[e] = (xr[c + 2][j] * cs + xr[c][j] * sn) * C2; }
	v_mov_b32_e32 v9, v32
	v_mov_b32_e32 v32, v25
	v_mov_b32_e32 v24, v22
	v_mov_b32_e32 v25, v30
	v_mov_b32_e32 v30, v23
	v_mov_b32_e32 v22, v20
	v_mov_b32_e32 v23, v28
	v_mov_b32_e32 v28, v21
	v_mov_b32_e32 v20, v18
	v_mov_b32_e32 v21, v26
	v_mov_b32_e32 v26, v19
	s_waitcnt vmcnt(2)
	v_mov_b32_e32 v18, v36
	s_waitcnt vmcnt(0)
	v_mov_b32_e32 v19, v44
	v_mov_b32_e32 v44, v37
	v_mov_b32_e32 v36, v34
	v_mov_b32_e32 v37, v42
	v_mov_b32_e32 v42, v35
	v_mov_b32_e32 v34, v14
	v_mov_b32_e32 v35, v40
	v_mov_b32_e32 v40, v15
	v_mov_b32_e32 v14, v12
	v_mov_b32_e32 v15, v38
	v_mov_b32_e32 v38, v13
	v_pk_mul_f32 v[12:13], v[14:15], v[2:3] op_sel_hi:[1,0]
	v_pk_mul_f32 v[14:15], v[38:39], v[2:3] op_sel_hi:[1,0]
	v_pk_mul_f32 v[34:35], v[34:35], v[2:3] op_sel_hi:[1,0]
	v_pk_mul_f32 v[38:39], v[40:41], v[2:3] op_sel_hi:[1,0]
	v_pk_mul_f32 v[36:37], v[36:37], v[2:3] op_sel_hi:[1,0]
	v_pk_mul_f32 v[40:41], v[42:43], v[2:3] op_sel_hi:[1,0]
	v_pk_mul_f32 v[42:43], v[44:45], v[2:3] op_sel_hi:[1,0]
	v_pk_mul_f32 v[26:27], v[26:27], v[2:3] op_sel_hi:[1,0]
	v_pk_mul_f32 v[28:29], v[28:29], v[2:3] op_sel_hi:[1,0]
	v_pk_mul_f32 v[24:25], v[2:3], v[24:25] op_sel_hi:[0,1]
	v_pk_mul_f32 v[30:31], v[2:3], v[30:31] op_sel_hi:[0,1]
	v_pk_mul_f32 v[8:9], v[2:3], v[8:9] op_sel_hi:[0,1]
	v_pk_mul_f32 v[32:33], v[2:3], v[32:33] op_sel_hi:[0,1]
	v_pk_mul_f32 v[18:19], v[18:19], v[2:3] op_sel_hi:[1,0]
	v_pk_mul_f32 v[20:21], v[20:21], v[2:3] op_sel_hi:[1,0]
	v_pk_mul_f32 v[22:23], v[22:23], v[2:3] op_sel_hi:[1,0]
	v_pk_mul_f32 v[4:5], v[14:15], v[4:5]
	v_pk_mul_f32 v[10:11], v[34:35], v[10:11]
	v_pk_mul_f32 v[14:15], v[38:39], v[66:67]
	v_pk_mul_f32 v[34:35], v[36:37], v[64:65]
	v_pk_mul_f32 v[6:7], v[40:41], v[6:7]
	v_pk_mul_f32 v[36:37], v[42:43], v[62:63]
	v_pk_mul_f32 v[16:17], v[26:27], v[16:17]
	v_pk_mul_f32 v[26:27], v[28:29], v[56:57]
	v_pk_mul_f32 v[24:25], v[24:25], v[50:51]
	v_pk_mul_f32 v[28:29], v[30:31], v[52:53]
	v_pk_mul_f32 v[8:9], v[8:9], v[46:47]
	v_pk_mul_f32 v[30:31], v[32:33], v[48:49]
	v_mul_f32_e32 v2, v192, v70
	v_mul_f32_e32 v32, v193, v70
	v_mul_f32_e32 v33, v194, v70
	v_mul_f32_e32 v38, v195, v70
	v_mul_f32_e32 v39, v196, v70
	v_mul_f32_e32 v40, v197, v70
	v_mul_f32_e32 v41, v198, v70
	v_mul_f32_e32 v42, v199, v70
	v_mul_f32_e32 v43, v200, v70
	v_mul_f32_e32 v44, v201, v70
	v_mul_f32_e32 v45, v202, v70
	v_mul_f32_e32 v46, v203, v70
	v_mul_f32_e32 v47, v204, v70
	v_mul_f32_e32 v48, v205, v70
	v_mul_f32_e32 v49, v206, v70
	v_mul_f32_e32 v50, v207, v70
	v_pk_mul_f32 v[18:19], v[18:19], v[60:61]
	v_pk_mul_f32 v[20:21], v[20:21], v[58:59]
	v_pk_mul_f32 v[22:23], v[22:23], v[54:55]
	v_mul_f32_e32 v51, 0.15915494, v2
	v_mul_f32_e32 v52, 0.15915494, v32
	v_mul_f32_e32 v53, 0.15915494, v33
	v_mul_f32_e32 v54, 0.15915494, v38
	v_mul_f32_e32 v55, 0.15915494, v39
	v_mul_f32_e32 v56, 0.15915494, v40
	v_mul_f32_e32 v57, 0.15915494, v41
	v_mul_f32_e32 v58, 0.15915494, v42
	v_mul_f32_e32 v59, 0.15915494, v43
	v_mul_f32_e32 v60, 0.15915494, v44
	v_mul_f32_e32 v61, 0.15915494, v45
	v_mul_f32_e32 v62, 0.15915494, v46
	v_mul_f32_e32 v63, 0.15915494, v47
	v_mul_f32_e32 v64, 0.15915494, v48
	v_mul_f32_e32 v65, 0.15915494, v49
	v_mul_f32_e32 v66, 0.15915494, v50
	v_floor_f32_e32 v51, v51
	v_floor_f32_e32 v52, v52
	v_floor_f32_e32 v53, v53
	v_floor_f32_e32 v54, v54
	v_floor_f32_e32 v55, v55
	v_floor_f32_e32 v56, v56
	v_floor_f32_e32 v57, v57
	v_floor_f32_e32 v58, v58
	v_floor_f32_e32 v59, v59
	v_floor_f32_e32 v60, v60
	v_floor_f32_e32 v61, v61
	v_floor_f32_e32 v62, v62
	v_floor_f32_e32 v63, v63
	v_floor_f32_e32 v64, v64
	v_floor_f32_e32 v65, v65
	v_floor_f32_e32 v66, v66
	v_fma_f32 v2, v2, 0.15915494, -v51
	v_fma_f32 v51, v32, 0.15915494, -v52
	v_fma_f32 v52, v33, 0.15915494, -v53
	v_fma_f32 v53, v38, 0.15915494, -v54
	v_fma_f32 v54, v39, 0.15915494, -v55
	v_fma_f32 v55, v40, 0.15915494, -v56
	v_fma_f32 v56, v41, 0.15915494, -v57
	v_fma_f32 v57, v42, 0.15915494, -v58
	v_fma_f32 v58, v43, 0.15915494, -v59
	v_fma_f32 v59, v44, 0.15915494, -v60
	v_fma_f32 v60, v45, 0.15915494, -v61
	v_fma_f32 v61, v46, 0.15915494, -v62
	v_fma_f32 v62, v47, 0.15915494, -v63
	v_fma_f32 v64, v48, 0.15915494, -v64
	v_fma_f32 v65, v49, 0.15915494, -v65
	v_fma_f32 v66, v50, 0.15915494, -v66
	v_sin_f32_e32 v32, v2
	v_cos_f32_e32 v33, v2
	v_sin_f32_e32 v39, v51
	v_cos_f32_e32 v38, v51
	v_sin_f32_e32 v40, v52
	v_cos_f32_e32 v41, v52
	v_sin_f32_e32 v43, v53
	v_cos_f32_e32 v42, v53
	v_sin_f32_e32 v44, v54
	v_cos_f32_e32 v45, v54
	v_sin_f32_e32 v47, v55
	v_cos_f32_e32 v46, v55
	v_sin_f32_e32 v48, v56
	v_cos_f32_e32 v49, v56
	v_sin_f32_e32 v51, v57
	v_cos_f32_e32 v50, v57
	v_sin_f32_e32 v52, v58
	v_cos_f32_e32 v53, v58
	v_sin_f32_e32 v55, v59
	v_cos_f32_e32 v54, v59
	v_sin_f32_e32 v56, v60
	v_cos_f32_e32 v57, v60
	v_sin_f32_e32 v59, v61
	v_cos_f32_e32 v58, v61
	v_sin_f32_e32 v60, v62
	v_cos_f32_e32 v61, v62
	v_sin_f32_e32 v63, v64
	v_cos_f32_e32 v62, v64
	v_sin_f32_e32 v64, v65
	v_cos_f32_e32 v65, v65
	v_sin_f32_e32 v67, v66
	v_cos_f32_e32 v66, v66
	v_pk_mul_f32 v[12:13], v[12:13], v[68:69]
	v_mov_b32_e32 v68, v33
	v_mov_b32_e32 v69, v32
	v_pk_mul_f32 v[32:33], v[32:33], v[12:13]
	v_pk_mul_f32 v[70:71], v[38:39], v[4:5]
	v_mov_b32_e32 v72, v39
	v_mov_b32_e32 v73, v38
	v_mov_b32_e32 v38, v41
	v_mov_b32_e32 v39, v40
	v_pk_mul_f32 v[74:75], v[42:43], v[14:15]
	v_mov_b32_e32 v76, v43
	v_mov_b32_e32 v77, v42
	v_mov_b32_e32 v42, v45
	v_mov_b32_e32 v43, v44
	v_pk_mul_f32 v[78:79], v[46:47], v[6:7]
	v_mov_b32_e32 v80, v47
; __device__ __forceinline__ unsigned cvtpk(float lo, float hi) { unsigned r; asm volatile("v_cvt_pk_bf16_f32 %0, %1, %2" : "=v"(r) : "v"(lo), "v"(hi)); return r; }
; template <int layer>
; __device__ __forceinline__ void attn_phase(LAS unsigned char* lds) {
;     ...
;                     for (int c = 0; c < 2; ++c) { u32x4 o1, o2;
; #pragma unroll
;                         for (int jj = 0; jj < 4; ++jj) { float y1[2], y2[2];
; #pragma unroll
;                             for (int e = 0; e < 2; ++e) { const int j = 2 * jj + e; const int i = c * 16 + hi * 8 + j;
;                                 const float freq = exp2f(-(float)i * (13.287712379549449f / 32.0f)); float rev = pos * freq * 0.15915494309189535f; rev -= floorf(rev);
;                                 const float sn = __builtin_amdgcn_sinf(rev), cs = __builtin_amdgcn_cosf(rev);
;                                 y1[e] = (xr[c][j] * cs - xr[c + 2][j] * sn) * C2; y2[e] = (xr[c + 2][j] * cs + xr[c][j] * sn) * C2; }
;                             o1[jj] = cvtpk(y1[0], y1[1]); o2[jj] = cvtpk(y2[0], y2[1]); }
;                         qr[8 + c] = *reinterpret_cast<bf16x8*>(&o1); qr[10 + c] = *reinterpret_cast<bf16x8*>(&o2); }
	v_mov_b32_e32 v81, v46
	v_mov_b32_e32 v46, v49
	v_mov_b32_e32 v47, v48
	v_pk_mul_f32 v[82:83], v[50:51], v[36:37]
	v_mov_b32_e32 v84, v51
	v_mov_b32_e32 v85, v50
	v_mov_b32_e32 v50, v53
	v_mov_b32_e32 v51, v52
	v_pk_mul_f32 v[86:87], v[54:55], v[16:17]
	v_mov_b32_e32 v88, v55
	v_mov_b32_e32 v89, v54
	v_mov_b32_e32 v54, v57
	v_mov_b32_e32 v55, v56
	v_pk_mul_f32 v[90:91], v[58:59], v[26:27]
	v_mov_b32_e32 v92, v59
	v_mov_b32_e32 v93, v58
	v_mov_b32_e32 v58, v61
	v_mov_b32_e32 v59, v60
	v_pk_mul_f32 v[94:95], v[62:63], v[28:29]
	v_mov_b32_e32 v96, v63
	v_mov_b32_e32 v97, v62
	v_mov_b32_e32 v62, v65
	v_mov_b32_e32 v63, v64
	v_mov_b32_e32 v100, v67
	v_mov_b32_e32 v101, v66
	v_pk_mul_f32 v[40:41], v[40:41], v[10:11]
	v_pk_mul_f32 v[44:45], v[44:45], v[34:35]
	v_pk_mul_f32 v[48:49], v[48:49], v[18:19]
	v_pk_mul_f32 v[52:53], v[52:53], v[20:21]
	v_pk_mul_f32 v[56:57], v[56:57], v[22:23]
	v_pk_mul_f32 v[60:61], v[60:61], v[24:25]
	v_pk_mul_f32 v[64:65], v[64:65], v[8:9]
	v_pk_mul_f32 v[98:99], v[66:67], v[30:31]
	v_pk_mul_f32 v[12:13], v[68:69], v[12:13]
	v_add_f32_e32 v2, v32, v33
	v_pk_mul_f32 v[4:5], v[72:73], v[4:5]
	v_pk_mul_f32 v[10:11], v[38:39], v[10:11]
	v_pk_mul_f32 v[14:15], v[76:77], v[14:15]
	v_pk_mul_f32 v[32:33], v[42:43], v[34:35]
	v_pk_mul_f32 v[6:7], v[80:81], v[6:7]
	v_pk_mul_f32 v[18:19], v[46:47], v[18:19]
	v_pk_mul_f32 v[34:35], v[84:85], v[36:37]
	v_pk_mul_f32 v[20:21], v[50:51], v[20:21]
	v_pk_mul_f32 v[16:17], v[88:89], v[16:17]
	v_pk_mul_f32 v[22:23], v[54:55], v[22:23]
	v_pk_mul_f32 v[26:27], v[92:93], v[26:27]
	v_pk_mul_f32 v[24:25], v[58:59], v[24:25]
	v_pk_mul_f32 v[28:29], v[96:97], v[28:29]
	v_pk_mul_f32 v[8:9], v[62:63], v[8:9]
	v_pk_mul_f32 v[30:31], v[100:101], v[30:31]
	v_sub_f32_e32 v66, v70, v71
	v_add_f32_e32 v38, v40, v41
	v_sub_f32_e32 v39, v74, v75
	v_add_f32_e32 v40, v44, v45
	v_sub_f32_e32 v41, v78, v79
	v_add_f32_e32 v42, v48, v49
	v_sub_f32_e32 v43, v82, v83
	v_add_f32_e32 v36, v52, v53
	v_sub_f32_e32 v37, v86, v87
	v_add_f32_e32 v44, v56, v57
	v_sub_f32_e32 v45, v90, v91
	v_add_f32_e32 v46, v60, v61
	v_sub_f32_e32 v47, v94, v95
	v_add_f32_e32 v48, v64, v65
	v_sub_f32_e32 v49, v98, v99
	v_sub_f32_e32 v12, v12, v13
	v_add_f32_e32 v4, v4, v5
	v_sub_f32_e32 v5, v10, v11
	v_add_f32_e32 v14, v14, v15
	v_sub_f32_e32 v15, v32, v33
	v_add_f32_e32 v6, v6, v7
	v_sub_f32_e32 v7, v18, v19
	v_add_f32_e32 v34, v34, v35
	v_sub_f32_e32 v20, v20, v21
	v_add_f32_e32 v16, v16, v17
	v_sub_f32_e32 v17, v22, v23
	v_add_f32_e32 v26, v26, v27
	v_sub_f32_e32 v24, v24, v25
	v_add_f32_e32 v28, v28, v29
	v_sub_f32_e32 v8, v8, v9
	v_add_f32_e32 v30, v30, v31
	v_mul_f32_e32 v2, 0x3dd53b94, v2
	v_mul_f32_e32 v13, 0x3dd53b94, v66
	v_mul_f32_e32 v10, 0x3dd53b94, v38
	v_mul_f32_e32 v11, 0x3dd53b94, v39
	v_mul_f32_e32 v32, 0x3dd53b94, v40
	v_mul_f32_e32 v33, 0x3dd53b94, v41
	v_mul_f32_e32 v18, 0x3dd53b94, v42
	v_mul_f32_e32 v19, 0x3dd53b94, v43
	v_mul_f32_e32 v21, 0x3dd53b94, v36
	v_mul_f32_e32 v35, 0x3dd53b94, v37
	v_mul_f32_e32 v22, 0x3dd53b94, v44
	v_mul_f32_e32 v23, 0x3dd53b94, v45
	v_mul_f32_e32 v25, 0x3dd53b94, v46
	v_mul_f32_e32 v27, 0x3dd53b94, v47
	v_mul_f32_e32 v9, 0x3dd53b94, v48
	v_mul_f32_e32 v29, 0x3dd53b94, v49
	v_mul_f32_e32 v12, 0x3dd53b94, v12
	v_mul_f32_e32 v4, 0x3dd53b94, v4
	v_mul_f32_e32 v5, 0x3dd53b94, v5
	v_mul_f32_e32 v14, 0x3dd53b94, v14
	v_mul_f32_e32 v15, 0x3dd53b94, v15
	v_mul_f32_e32 v6, 0x3dd53b94, v6
	v_mul_f32_e32 v7, 0x3dd53b94, v7
	v_mul_f32_e32 v31, 0x3dd53b94, v34
	v_mul_f32_e32 v20, 0x3dd53b94, v20
	v_mul_f32_e32 v16, 0x3dd53b94, v16
	v_mul_f32_e32 v17, 0x3dd53b94, v17
	v_mul_f32_e32 v26, 0x3dd53b94, v26
	v_mul_f32_e32 v24, 0x3dd53b94, v24
	v_mul_f32_e32 v28, 0x3dd53b94, v28
	v_mul_f32_e32 v8, 0x3dd53b94, v8
	v_mul_f32_e32 v30, 0x3dd53b94, v30
	v_cvt_pk_bf16_f32 v164, v12, v13
	v_cvt_pk_bf16_f32 v168, v2, v4
	v_cvt_pk_bf16_f32 v165, v5, v11
	v_cvt_pk_bf16_f32 v169, v10, v14
	v_cvt_pk_bf16_f32 v166, v15, v33
	v_cvt_pk_bf16_f32 v170, v32, v6
	v_cvt_pk_bf16_f32 v167, v7, v19
	v_cvt_pk_bf16_f32 v171, v18, v31
	v_cvt_pk_bf16_f32 v172, v20, v35
	v_cvt_pk_bf16_f32 v176, v21, v16
	v_cvt_pk_bf16_f32 v173, v17, v23
	v_cvt_pk_bf16_f32 v177, v22, v26
	v_cvt_pk_bf16_f32 v174, v24, v27
	v_cvt_pk_bf16_f32 v178, v25, v28
	v_cvt_pk_bf16_f32 v175, v8, v29
	v_cvt_pk_bf16_f32 v179, v9, v30
	s_cbranch_vccnz .LBB0_531
	s_mov_b32 s9, m0
	s_mov_b32 m0, s65
	s_nop 0
	global_load_lds_dwordx4 v1, s[34:35]
	s_mov_b32 m0, s9
	s_nop 0
	s_mov_b32 s9, m0
	s_mov_b32 m0, s73
	s_nop 0
	global_load_lds_dwordx4 v208, s[34:35]
	s_mov_b32 m0, s9
	s_nop 0
	s_mov_b32 s9, m0
	s_mov_b32 m0, s74
	s_nop 0
	global_load_lds_dwordx4 v209, s[34:35]
	s_mov_b32 m0, s9
	s_nop 0
	s_mov_b32 s9, m0
	s_mov_b32 m0, s75
	s_nop 0
	global_load_lds_dwordx4 v210, s[34:35]
	s_mov_b32 m0, s9
	s_nop 0
	s_mov_b32 s9, m0
	s_mov_b32 m0, s66
	s_nop 0
	global_load_lds_dwordx4 v188, s[38:39]
	s_mov_b32 m0, s9
	s_nop 0
	s_mov_b32 s9, m0
	s_mov_b32 m0, s76
	s_nop 0
	global_load_lds_dwordx4 v211, s[38:39]
	s_mov_b32 m0, s9
	s_nop 0
	s_mov_b32 s9, m0
	s_mov_b32 m0, s67
	s_nop 0
	global_load_lds_dwordx4 v181, s[36:37]
	s_mov_b32 m0, s9
	s_nop 0
	s_mov_b32 s9, m0
	s_mov_b32 m0, s64
	s_nop 0
	global_load_lds_dwordx4 v212, s[36:37]
	s_mov_b32 m0, s9
	s_nop 0
	s_mov_b32 s9, m0
	s_mov_b32 m0, s77
	s_nop 0
	global_load_lds_dwordx4 v213, s[36:37]
	s_mov_b32 m0, s9
	s_nop 0
	s_mov_b32 s9, m0
	s_mov_b32 m0, s78
	s_nop 0
	global_load_lds_dwordx4 v214, s[36:37]
	s_mov_b32 m0, s9

; __device__ __forceinline__ float bf2f(unsigned b) { return __uint_as_float(b << 16); }
; __device__ __forceinline__ float rsq(float x) { return __builtin_amdgcn_rsqf(x); }
; template <int layer>
; __device__ __forceinline__ void attn_phase(LAS unsigned char* lds) {
;     ...
;                 const size_t tq = (size_t)b * SEQ + qlo + r32;
;                 const bf16* qp = Qs + tq * QLD + h * QHS + hi * 8;
;                 u32x4 raw[NQ];
; #pragma unroll
;                 for (int d0 = 0; d0 < NQ; ++d0) raw[d0] = *(const u32x4*)(qp + d0 * 16);
;                 float ss = 0.f;
; #pragma unroll
;                 for (int d0 = 0; d0 < 8; ++d0)
; #pragma unroll
;                     for (int j = 0; j < 4; ++j) { const float x0 = bf2f(raw[d0][j] & 0xffffu), x1 = bf2f(raw[d0][j] >> 16); ss += x0 * x0 + x1 * x1; }
;                 { auto rr = __builtin_amdgcn_permlane32_swap(__float_as_uint(ss), __float_as_uint(ss), false, false); ss = __uint_as_float(rr[0]) + __uint_as_float(rr[1]); }
;                 const float rn = rsq(ss * (1.0f / 128) + EPS) * C2;
.LBB0_1422:
	s_and_b64 s[4:5], s[8:9], exec
	v_readlane_b32 s4, v252, 28
	v_readlane_b32 s5, v252, 31
	s_cselect_b32 s10, s5, s4
	v_readlane_b32 s4, v252, 23
	s_add_i32 s40, s10, s4
	s_ashr_i32 s4, s40, 31
	s_add_u32 s68, s34, s40
	s_addc_u32 s69, s35, s4
	v_mov_b32_e32 v5, s69
	v_or_b32_e32 v4, s68, v132
	v_lshlrev_b64 v[4:5], 14, v[4:5]
	v_lshl_add_u64 v[4:5], v[138:139], 0, v[4:5]
	global_load_dwordx4 v[20:23], v[4:5], off
	global_load_dwordx4 v[24:27], v[4:5], off offset:32
	global_load_dwordx4 v[28:31], v[4:5], off offset:64
	global_load_dwordx4 v[32:35], v[4:5], off offset:96
	global_load_dwordx4 v[16:19], v[4:5], off offset:128
	global_load_dwordx4 v[12:15], v[4:5], off offset:160
	global_load_dwordx4 v[8:11], v[4:5], off offset:192
	s_nop 0
	global_load_dwordx4 v[4:7], v[4:5], off offset:224
	v_cmp_ne_u32_e64 s[4:5], 1, v186
	s_andn2_b64 vcc, exec, s[20:21]
	v_cmp_ne_u32_e64 s[6:7], 1, v187
	s_waitcnt vmcnt(7)
	v_and_b32_e32 v36, 0xffff0000, v20
	v_and_b32_e32 v38, 0xffff0000, v21
	v_lshlrev_b32_e32 v2, 16, v20
	v_lshlrev_b32_e32 v37, 16, v21
	v_and_b32_e32 v40, 0xffff0000, v22
	v_mul_f32_e32 v20, v36, v36
	v_mul_f32_e32 v21, v38, v38
	v_lshlrev_b32_e32 v39, 16, v22
	v_and_b32_e32 v42, 0xffff0000, v23
	v_mul_f32_e32 v22, v40, v40
	v_fmac_f32_e32 v20, v2, v2
	v_fmac_f32_e32 v21, v37, v37
	v_lshlrev_b32_e32 v41, 16, v23
	s_waitcnt vmcnt(6)
	v_and_b32_e32 v44, 0xffff0000, v24
	v_mul_f32_e32 v23, v42, v42
	v_fmac_f32_e32 v22, v39, v39
	v_add_f32_e32 v20, v20, v21
	v_lshlrev_b32_e32 v43, 16, v24
	v_and_b32_e32 v46, 0xffff0000, v25
	v_mul_f32_e32 v24, v44, v44
	v_fmac_f32_e32 v23, v41, v41
	v_add_f32_e32 v20, v22, v20
	v_lshlrev_b32_e32 v45, 16, v25
	v_and_b32_e32 v48, 0xffff0000, v26
	v_mul_f32_e32 v25, v46, v46
	v_fmac_f32_e32 v24, v43, v43
	v_add_f32_e32 v20, v23, v20
	v_lshlrev_b32_e32 v47, 16, v26
	v_and_b32_e32 v50, 0xffff0000, v27
	v_mul_f32_e32 v26, v48, v48
	v_fmac_f32_e32 v25, v45, v45
	v_add_f32_e32 v20, v24, v20
	v_lshlrev_b32_e32 v49, 16, v27
	s_waitcnt vmcnt(5)
	v_lshlrev_b32_e32 v51, 16, v28
	v_and_b32_e32 v28, 0xffff0000, v28
	v_mul_f32_e32 v27, v50, v50
	v_fmac_f32_e32 v26, v47, v47
	v_add_f32_e32 v20, v25, v20
	v_lshlrev_b32_e32 v52, 16, v29
	v_and_b32_e32 v29, 0xffff0000, v29
	v_mul_f32_e32 v62, v28, v28
	v_fmac_f32_e32 v27, v49, v49
	v_add_f32_e32 v20, v26, v20
	v_lshlrev_b32_e32 v53, 16, v30
	v_and_b32_e32 v30, 0xffff0000, v30
	v_mul_f32_e32 v63, v29, v29
	v_fmac_f32_e32 v62, v51, v51
	v_add_f32_e32 v20, v27, v20
	v_lshlrev_b32_e32 v54, 16, v31
	v_and_b32_e32 v31, 0xffff0000, v31
	v_mul_f32_e32 v64, v30, v30
	v_fmac_f32_e32 v63, v52, v52
	v_add_f32_e32 v20, v62, v20
	s_waitcnt vmcnt(4)
	v_lshlrev_b32_e32 v55, 16, v32
	v_and_b32_e32 v32, 0xffff0000, v32
	v_mul_f32_e32 v65, v31, v31
	v_fmac_f32_e32 v64, v53, v53
	v_add_f32_e32 v20, v63, v20
	v_lshlrev_b32_e32 v56, 16, v33
	v_and_b32_e32 v33, 0xffff0000, v33
	v_mul_f32_e32 v66, v32, v32
	v_fmac_f32_e32 v65, v54, v54
	v_add_f32_e32 v20, v64, v20
	v_lshlrev_b32_e32 v57, 16, v34
	v_and_b32_e32 v34, 0xffff0000, v34
	v_mul_f32_e32 v67, v33, v33
	v_fmac_f32_e32 v66, v55, v55
	v_add_f32_e32 v20, v65, v20
	v_lshlrev_b32_e32 v58, 16, v35
	v_and_b32_e32 v35, 0xffff0000, v35
	v_mul_f32_e32 v68, v34, v34
	v_fmac_f32_e32 v67, v56, v56
	v_add_f32_e32 v20, v66, v20
	s_waitcnt vmcnt(3)
	v_lshlrev_b32_e32 v59, 16, v16
	v_and_b32_e32 v16, 0xffff0000, v16
	v_mul_f32_e32 v69, v35, v35
	v_fmac_f32_e32 v68, v57, v57
	v_add_f32_e32 v20, v67, v20
	v_lshlrev_b32_e32 v60, 16, v17
	v_and_b32_e32 v17, 0xffff0000, v17
	v_mul_f32_e32 v70, v16, v16
	v_fmac_f32_e32 v69, v58, v58
	v_add_f32_e32 v20, v68, v20
	v_mul_f32_e32 v71, v17, v17
	v_fmac_f32_e32 v70, v59, v59
	v_add_f32_e32 v20, v69, v20
	v_fmac_f32_e32 v71, v60, v60
	v_add_f32_e32 v20, v70, v20
	v_add_f32_e32 v62, v71, v20
	global_load_dwordx4 v[20:23], v[136:137], off offset:16
	global_load_dwordx4 v[24:27], v[136:137], off
	global_load_dwordx4 v[140:143], v[136:137], off offset:64
	global_load_dwordx4 v[144:147], v[136:137], off offset:80
	global_load_dwordx4 v[148:151], v[136:137], off offset:128
	global_load_dwordx4 v[152:155], v[136:137], off offset:144
	global_load_dwordx4 v[156:159], v[136:137], off offset:192
	global_load_dwordx4 v[160:163], v[136:137], off offset:208
	global_load_dwordx4 v[164:167], v[136:137], off offset:256
	global_load_dwordx4 v[168:171], v[136:137], off offset:272
	global_load_dwordx4 v[208:211], v[136:137], off offset:320
	global_load_dwordx4 v[212:215], v[136:137], off offset:336
	global_load_dwordx4 v[216:219], v[136:137], off offset:384
	global_load_dwordx4 v[220:223], v[136:137], off offset:400
	v_lshlrev_b32_e32 v61, 16, v18
	v_and_b32_e32 v18, 0xffff0000, v18
	v_mul_f32_e32 v63, v18, v18
	v_fmac_f32_e32 v63, v61, v61
	v_add_f32_e32 v62, v63, v62
	v_lshlrev_b32_e32 v63, 16, v19
	v_and_b32_e32 v19, 0xffff0000, v19
	v_mul_f32_e32 v64, v19, v19
	v_fmac_f32_e32 v64, v63, v63
	v_add_f32_e32 v62, v64, v62
	s_waitcnt vmcnt(16)
	v_lshlrev_b32_e32 v64, 16, v12
	v_and_b32_e32 v12, 0xffff0000, v12
	v_mul_f32_e32 v65, v12, v12
	v_fmac_f32_e32 v65, v64, v64
	v_add_f32_e32 v62, v65, v62
	v_lshlrev_b32_e32 v65, 16, v13
	v_and_b32_e32 v13, 0xffff0000, v13
	v_mul_f32_e32 v66, v13, v13
	v_fmac_f32_e32 v66, v65, v65
	v_add_f32_e32 v62, v66, v62
	v_lshlrev_b32_e32 v66, 16, v14
	v_and_b32_e32 v14, 0xffff0000, v14
	v_mul_f32_e32 v67, v14, v14
	v_fmac_f32_e32 v67, v66, v66
	v_add_f32_e32 v62, v67, v62
	v_lshlrev_b32_e32 v67, 16, v15
	v_and_b32_e32 v15, 0xffff0000, v15
	v_mul_f32_e32 v68, v15, v15
	v_fmac_f32_e32 v68, v67, v67
	s_waitcnt vmcnt(15)
; __device__ __forceinline__ float bf2f(unsigned b) { return __uint_as_float(b << 16); }
; __device__ __forceinline__ float rsq(float x) { return __builtin_amdgcn_rsqf(x); }
; __device__ __forceinline__ unsigned cvtpk(float lo, float hi) { unsigned r; asm volatile("v_cvt_pk_bf16_f32 %0, %1, %2" : "=v"(r) : "v"(lo), "v"(hi)); return r; }
; template <int layer>
; __device__ __forceinline__ void attn_phase(LAS unsigned char* lds) {
;     ...
;                 const float rn = rsq(ss * (1.0f / 128) + EPS) * C2;
; #pragma unroll
;                 for (int d0 = 0; d0 < 8; ++d0) { const f32x4 g0 = *(const f32x4*)(qkg + d0 * 16 + hi * 8), g1 = *(const f32x4*)(qkg + d0 * 16 + hi * 8 + 4); u32x4 o;
; #pragma unroll
;                     for (int j = 0; j < 4; ++j) { const float x0 = bf2f(raw[d0][j] & 0xffffu), x1 = bf2f(raw[d0][j] >> 16); const f32x4 gg = j < 2 ? g0 : g1;
;                         o[j] = cvtpk(x0 * rn * gg[(2 * j) & 3], x1 * rn * gg[(2 * j + 1) & 3]); }
;                     qr[d0] = *reinterpret_cast<bf16x8*>(&o); }
	v_and_b32_e32 v69, 0xffff0000, v8
	v_add_f32_e32 v62, v68, v62
	v_lshlrev_b32_e32 v68, 16, v8
	v_mul_f32_e32 v8, v69, v69
	v_fmac_f32_e32 v8, v68, v68
	v_and_b32_e32 v70, 0xffff0000, v9
	v_add_f32_e32 v8, v8, v62
	v_lshlrev_b32_e32 v62, 16, v9
	v_mul_f32_e32 v9, v70, v70
	v_fmac_f32_e32 v9, v62, v62
	v_and_b32_e32 v72, 0xffff0000, v10
	v_add_f32_e32 v8, v9, v8
	v_lshlrev_b32_e32 v71, 16, v10
	v_mul_f32_e32 v9, v72, v72
	v_fmac_f32_e32 v9, v71, v71
	v_and_b32_e32 v74, 0xffff0000, v11
	v_add_f32_e32 v8, v9, v8
	v_lshlrev_b32_e32 v73, 16, v11
	v_mul_f32_e32 v9, v74, v74
	s_waitcnt vmcnt(14)
	v_and_b32_e32 v76, 0xffff0000, v4
	v_fmac_f32_e32 v9, v73, v73
	v_lshlrev_b32_e32 v75, 16, v4
	v_mul_f32_e32 v4, v76, v76
	v_and_b32_e32 v78, 0xffff0000, v5
	v_add_f32_e32 v8, v9, v8
	v_fmac_f32_e32 v4, v75, v75
	v_lshlrev_b32_e32 v77, 16, v5
	v_mul_f32_e32 v5, v78, v78
	v_add_f32_e32 v4, v4, v8
	v_fmac_f32_e32 v5, v77, v77
	v_and_b32_e32 v80, 0xffff0000, v6
	v_add_f32_e32 v4, v5, v4
	v_lshlrev_b32_e32 v79, 16, v6
	v_mul_f32_e32 v5, v80, v80
	v_fmac_f32_e32 v5, v79, v79
	v_and_b32_e32 v82, 0xffff0000, v7
	v_add_f32_e32 v4, v5, v4
	v_lshlrev_b32_e32 v81, 16, v7
	v_mul_f32_e32 v5, v82, v82
	v_fmac_f32_e32 v5, v81, v81
	v_add_f32_e32 v4, v5, v4
	v_mov_b32_e32 v5, v4
	s_nop 1
	v_permlane32_swap_b32_e32 v4, v5
	v_add_f32_e32 v4, v4, v5
	v_fmamk_f32 v4, v4, 0x3c000000, v185
	v_rsq_f32_e32 v4, v4
	s_nop 0
	v_mul_f32_e32 v83, 0x3e0293ee, v4
	v_mul_f32_e32 v4, v83, v36
	v_mul_f32_e32 v2, v83, v2
	s_waitcnt vmcnt(12)
	v_mul_f32_e32 v4, v25, v4
	v_mul_f32_e32 v2, v24, v2
	v_cvt_pk_bf16_f32 v100, v2, v4
	v_mul_f32_e32 v4, v83, v38
	v_mul_f32_e32 v2, v83, v37
	v_mul_f32_e32 v4, v27, v4
	v_mul_f32_e32 v2, v26, v2
	v_cvt_pk_bf16_f32 v101, v2, v4
	v_mul_f32_e32 v4, v83, v40
	v_mul_f32_e32 v2, v83, v39
	v_mul_f32_e32 v4, v21, v4
	v_mul_f32_e32 v2, v20, v2
	v_cvt_pk_bf16_f32 v102, v2, v4
	v_mul_f32_e32 v4, v83, v42
	v_mul_f32_e32 v2, v83, v41
	v_mul_f32_e32 v4, v23, v4
	v_mul_f32_e32 v2, v22, v2
	v_cvt_pk_bf16_f32 v103, v2, v4
	global_load_dwordx4 v[4:7], v[136:137], off offset:448
	global_load_dwordx4 v[8:11], v[136:137], off offset:464
	v_mul_f32_e32 v2, v83, v43
	v_mul_f32_e32 v20, v83, v44
	v_mul_f32_e32 v22, v83, v46
	v_mul_f32_e32 v21, v83, v45
	v_mul_f32_e32 v23, v83, v53
	v_mul_f32_e32 v24, v83, v30
	v_mul_f32_e32 v25, v83, v54
	v_mul_f32_e32 v26, v83, v31
	v_mul_f32_e32 v16, v83, v16
	v_mul_f32_e32 v17, v83, v17
	v_mul_f32_e32 v18, v83, v18
	v_mul_f32_e32 v19, v83, v19
	v_mul_f32_e32 v12, v83, v12
	v_mul_f32_e32 v13, v83, v13
	v_mul_f32_e32 v14, v83, v14
	v_mul_f32_e32 v15, v83, v15
	s_waitcnt vmcnt(13)
	v_mul_f32_e32 v2, v140, v2
	v_mul_f32_e32 v140, v141, v20
	v_cvt_pk_bf16_f32 v104, v2, v140
	v_mul_f32_e32 v2, v143, v22
	v_mul_f32_e32 v140, v83, v48
	v_mul_f32_e32 v141, v142, v21
	v_cvt_pk_bf16_f32 v105, v141, v2
	v_mul_f32_e32 v2, v83, v47
	s_waitcnt vmcnt(12)
	v_mul_f32_e32 v140, v140, v145
	v_mul_f32_e32 v2, v2, v144
	v_cvt_pk_bf16_f32 v106, v2, v140
	v_mul_f32_e32 v140, v83, v50
	v_mul_f32_e32 v2, v83, v49
	v_mul_f32_e32 v140, v140, v147
	v_mul_f32_e32 v2, v2, v146
	v_cvt_pk_bf16_f32 v107, v2, v140
	v_mul_f32_e32 v2, v83, v51
	v_mul_f32_e32 v20, v83, v28
	v_mul_f32_e32 v21, v83, v52
	v_mul_f32_e32 v22, v83, v29
	s_waitcnt vmcnt(11)
	v_mul_f32_e32 v2, v2, v148
	v_mul_f32_e32 v148, v20, v149
	v_mul_f32_e32 v149, v21, v150
	v_mul_f32_e32 v150, v22, v151
	s_waitcnt vmcnt(10)
	v_mul_f32_e32 v151, v23, v152
	v_mul_f32_e32 v152, v24, v153
	v_mul_f32_e32 v153, v25, v154
	v_mul_f32_e32 v154, v26, v155
	v_cvt_pk_bf16_f32 v108, v2, v148
	v_cvt_pk_bf16_f32 v109, v149, v150
	v_cvt_pk_bf16_f32 v110, v151, v152
	v_cvt_pk_bf16_f32 v111, v153, v154
	v_mul_f32_e32 v2, v83, v55
	v_mul_f32_e32 v20, v83, v32
	v_mul_f32_e32 v21, v83, v56
	v_mul_f32_e32 v22, v83, v33
	v_mul_f32_e32 v23, v83, v57
	v_mul_f32_e32 v24, v83, v34
	v_mul_f32_e32 v25, v83, v58
	v_mul_f32_e32 v26, v83, v35
	s_waitcnt vmcnt(9)
	v_mul_f32_e32 v2, v2, v156
	v_mul_f32_e32 v156, v20, v157
	v_mul_f32_e32 v157, v21, v158
	v_mul_f32_e32 v158, v22, v159
	s_waitcnt vmcnt(8)
	v_mul_f32_e32 v159, v23, v160
	v_mul_f32_e32 v160, v24, v161
	v_mul_f32_e32 v161, v25, v162
	v_mul_f32_e32 v162, v26, v163
	v_cvt_pk_bf16_f32 v112, v2, v156
	v_cvt_pk_bf16_f32 v113, v157, v158
	v_cvt_pk_bf16_f32 v114, v159, v160
	v_cvt_pk_bf16_f32 v115, v161, v162
	v_mul_f32_e32 v2, v83, v59
	v_mul_f32_e32 v20, v83, v60
	v_mul_f32_e32 v21, v83, v61
	v_mul_f32_e32 v22, v83, v63
	s_waitcnt vmcnt(7)
	v_mul_f32_e32 v2, v2, v164
	v_mul_f32_e32 v164, v16, v165
	v_mul_f32_e32 v165, v20, v166
	v_mul_f32_e32 v166, v17, v167
	s_waitcnt vmcnt(6)
	v_mul_f32_e32 v167, v21, v168
	v_mul_f32_e32 v168, v18, v169
	v_mul_f32_e32 v169, v22, v170
	v_mul_f32_e32 v170, v19, v171
	v_cvt_pk_bf16_f32 v116, v2, v164
	v_cvt_pk_bf16_f32 v117, v165, v166
	v_cvt_pk_bf16_f32 v118, v167, v168
	v_cvt_pk_bf16_f32 v119, v169, v170
	v_mul_f32_e32 v2, v83, v64
	v_mul_f32_e32 v16, v83, v65
	v_mul_f32_e32 v17, v83, v66
	v_mul_f32_e32 v18, v83, v67
	s_waitcnt vmcnt(5)
	v_mul_f32_e32 v2, v2, v208
	v_mul_f32_e32 v208, v12, v209
	v_mul_f32_e32 v209, v16, v210
	v_mul_f32_e32 v210, v13, v211
	s_waitcnt vmcnt(4)
	v_mul_f32_e32 v211, v17, v212
	v_mul_f32_e32 v212, v14, v213
	v_mul_f32_e32 v213, v18, v214
	v_mul_f32_e32 v214, v15, v215
	v_cvt_pk_bf16_f32 v120, v2, v208
	v_cvt_pk_bf16_f32 v121, v209, v210
	v_cvt_pk_bf16_f32 v122, v211, v212
	v_cvt_pk_bf16_f32 v123, v213, v214
	v_mul_f32_e32 v2, v83, v68
	v_mul_f32_e32 v12, v83, v69
	v_mul_f32_e32 v13, v83, v62
	v_mul_f32_e32 v14, v83, v70
	v_mul_f32_e32 v15, v83, v71
	v_mul_f32_e32 v16, v83, v72
	v_mul_f32_e32 v17, v83, v73
	v_mul_f32_e32 v18, v83, v74
	s_waitcnt vmcnt(3)
	v_mul_f32_e32 v2, v2, v216
	v_mul_f32_e32 v216, v12, v217
	v_mul_f32_e32 v217, v13, v218
	v_mul_f32_e32 v218, v14, v219
	s_waitcnt vmcnt(2)
	v_mul_f32_e32 v219, v15, v220
	v_mul_f32_e32 v220, v16, v221
	v_mul_f32_e32 v221, v17, v222
	v_mul_f32_e32 v222, v18, v223
	v_cvt_pk_bf16_f32 v124, v2, v216
	v_cvt_pk_bf16_f32 v125, v217, v218
	v_cvt_pk_bf16_f32 v126, v219, v220
	v_cvt_pk_bf16_f32 v127, v221, v222
	v_mul_f32_e32 v2, v83, v75
	v_mul_f32_e32 v12, v83, v76
	v_mul_f32_e32 v13, v83, v77
	v_mul_f32_e32 v14, v83, v78
	v_mul_f32_e32 v15, v83, v79
	v_mul_f32_e32 v16, v83, v80
	v_mul_f32_e32 v17, v83, v81
	v_mul_f32_e32 v18, v83, v82
	s_waitcnt vmcnt(1)
	v_mul_f32_e32 v2, v2, v4
	v_mul_f32_e32 v4, v12, v5
	v_mul_f32_e32 v5, v13, v6
	v_mul_f32_e32 v6, v14, v7
	s_waitcnt vmcnt(0)
	v_mul_f32_e32 v7, v15, v8
	v_mul_f32_e32 v8, v16, v9
	v_mul_f32_e32 v9, v17, v10
	v_mul_f32_e32 v10, v18, v11
	v_cvt_pk_bf16_f32 v128, v2, v4
	v_cvt_pk_bf16_f32 v129, v5, v6
	v_cvt_pk_bf16_f32 v130, v7, v8
	v_cvt_pk_bf16_f32 v131, v9, v10
	s_cbranch_vccnz .LBB0_1425
	s_mov_b32 s11, m0
	s_mov_b32 m0, s77
	s_nop 0
	global_load_lds_dwordx4 v1, s[36:37]
	s_mov_b32 m0, s11
	s_and_b64 vcc, exec, s[6:7]
	s_mov_b32 s11, m0
	s_mov_b32 m0, s84
	s_nop 0
	global_load_lds_dwordx4 v178, s[36:37]
	s_mov_b32 m0, s11
	s_nop 0
	s_mov_b32 s11, m0
	s_mov_b32 m0, s85
	s_nop 0
	global_load_lds_dwordx4 v179, s[36:37]
	s_mov_b32 m0, s11
	s_nop 0
	s_mov_b32 s11, m0
	s_mov_b32 m0, s86
	s_nop 0
	global_load_lds_dwordx4 v180, s[36:37]
	s_mov_b32 m0, s11
	s_nop 0
	s_mov_b32 s11, m0
	s_mov_b32 m0, s78
	s_nop 0
	global_load_lds_dwordx4 v133, s[38:39]
	s_mov_b32 m0, s11
	s_nop 0
	s_mov_b32 s11, m0
	s_mov_b32 m0, s76
	s_nop 0
	global_load_lds_dwordx4 v181, s[38:39]
	s_mov_b32 m0, s11
	s_nop 0
	s_mov_b32 s11, m0
	s_mov_b32 m0, s87
	s_nop 0
	global_load_lds_dwordx4 v182, s[38:39]
	s_mov_b32 m0, s11
	s_nop 0
	s_mov_b32 s11, m0
	s_mov_b32 m0, s88
	s_nop 0
	global_load_lds_dwordx4 v183, s[38:39]
	s_mov_b32 m0, s11
	s_cbranch_vccnz .LBB0_1425
	v_readlane_b32 s18, v252, 24
	v_readlane_b32 s19, v252, 25
	s_mov_b32 s11, m0
	s_mov_b32 m0, s81
	s_nop 0
	global_load_lds_dword v175, s[18:19]
	s_mov_b32 m0, s11
